# attention: PV fragment waits paired per 2 MFMAs, QK waits 8 per block
# baseline (speedup 1.0000x reference)
.LBB0_1173:
	s_mul_hi_u32 s7, s80, 0xaaaaaaab
	s_lshr_b32 s7, s7, 1
	s_mul_i32 s7, s7, 0xfffee000
	s_add_i32 s7, s7, 0
	v_add_u32_e32 v166, s6, v159
	v_add_u32_e32 v167, s6, v161
	v_add_u32_e32 v185, s6, v162
	v_add_u32_e32 v230, s6, v163
	ds_read_b128 v[66:69], v166 offset:32768
	ds_read_b128 v[82:85], v167 offset:32768
	ds_read_b128 v[86:89], v185 offset:32768
	ds_read_b128 v[90:93], v230 offset:32768
	ds_read_b128 v[94:97], v166 offset:32896
	ds_read_b128 v[186:189], v167 offset:32896
	ds_read_b128 v[190:193], v185 offset:32896
	ds_read_b128 v[194:197], v230 offset:32896
	ds_read_b128 v[198:201], v158
	ds_read_b128 v[202:205], v166 offset:33024
	ds_read_b128 v[206:209], v158 offset:1024
	ds_read_b128 v[210:213], v167 offset:33024
	ds_read_b128 v[214:217], v158 offset:2048
	ds_read_b128 v[218:221], v185 offset:33024
	ds_read_b128 v[222:225], v158 offset:3072
	s_waitcnt lgkmcnt(14)
	v_mfma_f32_32x32x16_bf16 v[66:81], v[66:69], v[126:129], 0
	ds_read_b128 v[226:229], v230 offset:33024
	s_waitcnt lgkmcnt(13)
	v_mfma_f32_32x32x16_bf16 v[66:81], v[82:85], v[122:125], v[66:81]
	v_mfma_f32_32x32x16_bf16 v[66:81], v[86:89], v[118:121], v[66:81]
	s_waitcnt lgkmcnt(11)
	v_mfma_f32_32x32x16_bf16 v[66:81], v[90:93], v[114:117], v[66:81]
	v_mfma_f32_32x32x16_bf16 v[66:81], v[94:97], v[110:113], v[66:81]
	s_waitcnt lgkmcnt(8)
	v_mfma_f32_32x32x16_bf16 v[66:81], v[186:189], v[106:109], v[66:81]
	ds_read_b128 v[186:189], v166 offset:45056
	v_mfma_f32_32x32x16_bf16 v[66:81], v[190:193], v[102:105], v[66:81]
	ds_read_b128 v[190:193], v167 offset:45056
	v_mfma_f32_32x32x16_bf16 v[66:81], v[194:197], v[98:101], v[66:81]
	ds_read_b128 v[194:197], v185 offset:45056
	s_waitcnt lgkmcnt(3)
	v_mfma_f32_32x32x16_bf16 v[66:81], v[202:205], v[198:201], v[66:81]
	ds_read_b128 v[202:205], v230 offset:45056
	v_mfma_f32_32x32x16_bf16 v[66:81], v[210:213], v[206:209], v[66:81]
	ds_read_b128 v[210:213], v166 offset:45184
	v_mfma_f32_32x32x16_bf16 v[66:81], v[218:221], v[214:217], v[66:81]
	ds_read_b128 v[218:221], v167 offset:45184
	v_mfma_f32_32x32x16_bf16 v[66:81], v[226:229], v[222:225], v[66:81]
	ds_read_b128 v[226:229], v185 offset:45184
	s_waitcnt lgkmcnt(3)
	v_mfma_f32_32x32x16_bf16 v[82:97], v[186:189], v[126:129], 0
	ds_read_b128 v[186:189], v230 offset:45184
	s_add_i32 s6, s78, 1
	s_min_u32 s6, s6, s14
	v_mfma_f32_32x32x16_bf16 v[82:97], v[190:193], v[122:125], v[82:97]
	ds_read_b128 v[246:249], v166 offset:45312
	s_lshl_b32 s10, s6, 6
	v_mfma_f32_32x32x16_bf16 v[82:97], v[194:197], v[118:121], v[82:97]
	ds_read_b128 v[242:245], v167 offset:45312
	s_cmp_lt_u32 s6, 4
	s_cselect_b32 s6, s74, s15
	s_add_i32 s6, s6, s10
	v_mfma_f32_32x32x16_bf16 v[82:97], v[202:205], v[114:117], v[82:97]
	ds_read_b128 v[238:241], v185 offset:45312
	s_mul_hi_i32 s11, s6, 0x1080
	s_mulk_i32 s6, 0x1080
	s_waitcnt lgkmcnt(3)
	v_mfma_f32_32x32x16_bf16 v[82:97], v[210:213], v[110:113], v[82:97]
	ds_read_b128 v[234:237], v230 offset:45312
	s_add_u32 s10, s3, s6
	s_addc_u32 s11, s35, s11
	s_add_i32 s6, s7, s30
	v_mfma_f32_32x32x16_bf16 v[82:97], v[218:221], v[106:109], v[82:97]
	s_add_i32 s6, s6, s8
	s_add_i32 m0, s6, 0x1a000
	s_nop 0
	global_load_lds_dwordx4 v232, s[10:11]
	v_mfma_f32_32x32x16_bf16 v[82:97], v[226:229], v[102:105], v[82:97]
	s_add_i32 m0, s6, 0x1a400
	v_mfma_f32_32x32x16_bf16 v[82:97], v[186:189], v[98:101], v[82:97]
	global_load_lds_dwordx4 v251, s[10:11]
	s_add_i32 m0, s6, 0x1a800
	s_waitcnt lgkmcnt(0)
	v_mfma_f32_32x32x16_bf16 v[82:97], v[246:249], v[198:201], v[82:97]
	v_mfma_f32_32x32x16_bf16 v[82:97], v[242:245], v[206:209], v[82:97]
	global_load_lds_dwordx4 v252, s[10:11]
	v_mfma_f32_32x32x16_bf16 v[82:97], v[238:241], v[214:217], v[82:97]
	v_mfma_f32_32x32x16_bf16 v[82:97], v[234:237], v[222:225], v[82:97]
	v_exp_f32_e32 v194, v130
	v_add_f32_e32 v130, 0, v178
	v_add_f32_e32 v130, v182, v130
	v_add_f32_e32 v130, v179, v130
	v_add_f32_e32 v130, v183, v130
	v_add_f32_e32 v130, v180, v130
	v_add_f32_e32 v130, v184, v130
	v_add_f32_e32 v130, v177, v130
	v_add_f32_e32 v130, v181, v130
	v_add_f32_e32 v130, v171, v130
	v_add_f32_e32 v130, v175, v130
	v_add_f32_e32 v130, v172, v130
	v_add_f32_e32 v130, v176, v130
	v_exp_f32_e32 v146, v146
	v_add_f32_e32 v130, v168, v130
	v_exp_f32_e32 v147, v147
	v_add_f32_e32 v130, v173, v130
	v_exp_f32_e32 v167, v144
	v_add_f32_e32 v130, v169, v130
	v_exp_f32_e32 v185, v145
	v_add_f32_e32 v130, v174, v130
	v_exp_f32_e32 v186, v142
	v_add_f32_e32 v130, v146, v130
	v_exp_f32_e32 v187, v143
	v_add_f32_e32 v130, v147, v130
	v_exp_f32_e32 v188, v140
	v_add_f32_e32 v130, v167, v130
	v_exp_f32_e32 v189, v141
	v_add_f32_e32 v130, v185, v130
	v_exp_f32_e32 v190, v138
	v_add_f32_e32 v130, v186, v130
	v_exp_f32_e32 v191, v139
	v_add_f32_e32 v130, v187, v130
	v_exp_f32_e32 v192, v136
	v_add_f32_e32 v130, v188, v130
	v_exp_f32_e32 v193, v137
	v_add_f32_e32 v130, v189, v130
	v_exp_f32_e32 v132, v132
	v_add_f32_e32 v130, v190, v130
	v_exp_f32_e32 v133, v133
	v_add_f32_e32 v130, v191, v130
	v_add_f32_e32 v130, v192, v130
	v_exp_f32_e32 v195, v131
	v_add_f32_e32 v130, v193, v130
	v_add_f32_e32 v130, v132, v130
	v_add_f32_e32 v130, v133, v130
	v_add_f32_e32 v130, v194, v130
	v_add_f32_e32 v136, v195, v130
	v_mov_b32_e32 v137, v136
	v_cvt_pk_bf16_f32 v138, v178, v182
	v_cvt_pk_bf16_f32 v139, v179, v183
	v_cvt_pk_bf16_f32 v140, v180, v184
	v_cvt_pk_bf16_f32 v141, v177, v181
	v_cvt_pk_bf16_f32 v142, v171, v175
	v_cvt_pk_bf16_f32 v143, v172, v176
	v_cvt_pk_bf16_f32 v144, v168, v173
	v_cvt_pk_bf16_f32 v145, v169, v174
	v_cvt_pk_bf16_f32 v166, v146, v147
	v_cvt_pk_bf16_f32 v167, v167, v185
	v_cvt_pk_bf16_f32 v168, v186, v187
	v_cvt_pk_bf16_f32 v169, v188, v189
	s_nop 1
	v_permlane32_swap_b32_e32 v136, v137
	v_permlane32_swap_b32_e32 v138, v140
	v_permlane32_swap_b32_e32 v167, v169
	v_cvt_pk_bf16_f32 v130, v190, v191
	v_cvt_pk_bf16_f32 v131, v192, v193
	v_cvt_pk_bf16_f32 v132, v132, v133
	v_cvt_pk_bf16_f32 v133, v194, v195
	v_permlane32_swap_b32_e32 v139, v141
	v_permlane32_swap_b32_e32 v142, v144
	v_permlane32_swap_b32_e32 v143, v145
	v_permlane32_swap_b32_e32 v166, v168
	v_permlane32_swap_b32_e32 v130, v132
	v_permlane32_swap_b32_e32 v131, v133
	ds_read_b64_tr_b16 v[172:173], v160 offset:0
	ds_read_b64_tr_b16 v[174:175], v160 offset:0x800
	ds_read_b64_tr_b16 v[176:177], v160 offset:0x1000
	ds_read_b64_tr_b16 v[178:179], v160 offset:0x1800
	ds_read_b64_tr_b16 v[180:181], v160 offset:0x2000
	ds_read_b64_tr_b16 v[182:183], v160 offset:0x2800
	ds_read_b64_tr_b16 v[184:185], v160 offset:0x3000
	ds_read_b64_tr_b16 v[186:187], v160 offset:0x3800
	s_nop 0
	s_waitcnt lgkmcnt(4)
	v_mfma_f32_32x32x16_bf16 v[2:17], v[138:141], v[172:175], v[2:17]
	ds_read_b64_tr_b16 v[172:173], v160 offset:0x200
	ds_read_b64_tr_b16 v[174:175], v160 offset:0xa00
	v_mfma_f32_32x32x16_bf16 v[2:17], v[142:145], v[176:179], v[2:17]
	ds_read_b64_tr_b16 v[176:177], v160 offset:0x1200
	ds_read_b64_tr_b16 v[178:179], v160 offset:0x1a00
	s_waitcnt lgkmcnt(4)
	v_mfma_f32_32x32x16_bf16 v[2:17], v[166:169], v[180:183], v[2:17]
	ds_read_b64_tr_b16 v[180:181], v160 offset:0x2200
	ds_read_b64_tr_b16 v[182:183], v160 offset:0x2a00
	ds_read_b64_tr_b16 v[188:189], v160 offset:0x3200
	ds_read_b64_tr_b16 v[190:191], v160 offset:0x3a00
	v_mfma_f32_32x32x16_bf16 v[2:17], v[130:133], v[184:187], v[2:17]
	s_waitcnt lgkmcnt(4)
	v_mfma_f32_32x32x16_bf16 v[50:65], v[138:141], v[172:175], v[50:65]
	ds_read_b64_tr_b16 v[172:173], v160 offset:0x400
	ds_read_b64_tr_b16 v[174:175], v160 offset:0xc00
	v_mfma_f32_32x32x16_bf16 v[50:65], v[142:145], v[176:179], v[50:65]
	ds_read_b64_tr_b16 v[176:177], v160 offset:0x1400
	ds_read_b64_tr_b16 v[178:179], v160 offset:0x1c00
	s_waitcnt lgkmcnt(4)
	v_mfma_f32_32x32x16_bf16 v[50:65], v[166:169], v[180:183], v[50:65]
	ds_read_b64_tr_b16 v[180:181], v160 offset:0x2400
	ds_read_b64_tr_b16 v[182:183], v160 offset:0x2c00
	ds_read_b64_tr_b16 v[184:185], v160 offset:0x3400
	ds_read_b64_tr_b16 v[186:187], v160 offset:0x3c00
	v_mfma_f32_32x32x16_bf16 v[50:65], v[130:133], v[188:191], v[50:65]
	s_waitcnt lgkmcnt(4)
	v_mfma_f32_32x32x16_bf16 v[34:49], v[138:141], v[172:175], v[34:49]
	ds_read_b64_tr_b16 v[172:173], v160 offset:0x600
	ds_read_b64_tr_b16 v[174:175], v160 offset:0xe00
	v_mfma_f32_32x32x16_bf16 v[34:49], v[142:145], v[176:179], v[34:49]
	ds_read_b64_tr_b16 v[176:177], v160 offset:0x1600
	ds_read_b64_tr_b16 v[178:179], v160 offset:0x1e00
	s_waitcnt lgkmcnt(4)
	v_mfma_f32_32x32x16_bf16 v[34:49], v[166:169], v[180:183], v[34:49]
	ds_read_b64_tr_b16 v[180:181], v160 offset:0x2600
	ds_read_b64_tr_b16 v[182:183], v160 offset:0x2e00
	ds_read_b64_tr_b16 v[188:189], v160 offset:0x3600
	ds_read_b64_tr_b16 v[190:191], v160 offset:0x3e00
	v_mfma_f32_32x32x16_bf16 v[34:49], v[130:133], v[184:187], v[34:49]
	v_max_f32_e32 v146, v67, v67
	v_max_f32_e32 v147, v66, v66
	v_max_f32_e32 v146, v147, v146
	v_max3_f32 v146, v146, v68, v69
	v_max3_f32 v146, v146, v70, v71
	s_waitcnt lgkmcnt(4)
	v_mfma_f32_32x32x16_bf16 v[18:33], v[138:141], v[172:175], v[18:33]
	v_max3_f32 v138, v146, v72, v73
	v_max3_f32 v138, v138, v74, v75
	v_max3_f32 v138, v138, v76, v77
	v_max3_f32 v138, v138, v78, v79
	v_max3_f32 v138, v138, v80, v81
	v_max3_f32 v138, v138, v82, v83
	v_max3_f32 v138, v138, v84, v85
	v_max3_f32 v138, v138, v86, v87
	v_max3_f32 v138, v138, v88, v89
	v_max3_f32 v138, v138, v90, v91
	v_max3_f32 v138, v138, v92, v93
	v_max3_f32 v138, v138, v94, v95
	v_max3_f32 v138, v138, v96, v97
	v_mov_b32_e32 v139, v138
	s_nop 1
	v_permlane32_swap_b32_e32 v138, v139
	v_max_f32_e32 v139, v139, v139
	v_max_f32_e32 v138, v138, v138
	v_max_f32_e32 v138, v138, v139
	v_sub_f32_e32 v139, v138, v165
	v_mfma_f32_32x32x16_bf16 v[18:33], v[142:145], v[176:179], v[18:33]
	v_cmp_ge_f32_e32 vcc, s65, v139
	s_waitcnt vmcnt(3) lgkmcnt(0)
	s_barrier
	s_cmp_eq_u64 vcc, exec
	s_cselect_b64 s[6:7], -1, 0
	s_cmp_lt_u32 s78, 4
	s_cselect_b32 s12, s74, s15
	s_add_i32 s12, s12, s9
	s_mul_hi_i32 s13, s12, 0x1080
	s_mulk_i32 s12, 0x1080
	s_add_u32 s12, s3, s12
	s_mov_b32 m0, s70
	s_addc_u32 s13, s35, s13
	global_load_lds_dwordx4 v253, s[12:13]
	s_mov_b32 m0, s72
	v_mfma_f32_32x32x16_bf16 v[18:33], v[166:169], v[180:183], v[18:33]
	global_load_lds_dwordx4 v254, s[12:13]
	v_max_f32_e32 v139, v165, v165
	v_max_f32_e32 v138, v139, v138
	v_sub_f32_e32 v139, v165, v138
	v_mul_f32_e32 v139, 0x3dd53b94, v139
	v_exp_f32_e32 v139, v139
	v_mfma_f32_32x32x16_bf16 v[18:33], v[130:133], v[188:191], v[18:33]
	v_cndmask_b32_e64 v167, v139, 1.0, s[6:7]
	v_cmp_gt_f32_e32 vcc, 1.0, v167
	s_cbranch_vccz .LBB0_1177
	s_and_saveexec_b64 s[12:13], s[4:5]
	ds_write_b32 v155, v167 offset:128
	s_or_b64 exec, exec, s[12:13]
	s_waitcnt lgkmcnt(0)
	v_add_u32_e32 v139, s69, v134
	ds_read_b128 v[130:133], v139 offset:224
	ds_read_b128 v[140:143], v139 offset:192
	ds_read_b128 v[144:147], v139 offset:160
	ds_read_b128 v[172:175], v139 offset:128
	s_waitcnt lgkmcnt(0)
	v_pk_mul_f32 v[14:15], v[14:15], v[130:131]
	v_pk_mul_f32 v[10:11], v[10:11], v[140:141]
	v_pk_mul_f32 v[6:7], v[6:7], v[144:145]
	v_pk_mul_f32 v[16:17], v[16:17], v[132:133]
	v_pk_mul_f32 v[12:13], v[12:13], v[142:143]
	v_pk_mul_f32 v[8:9], v[8:9], v[146:147]
	v_pk_mul_f32 v[4:5], v[4:5], v[174:175]
	v_pk_mul_f32 v[2:3], v[2:3], v[172:173]
	v_pk_mul_f32 v[62:63], v[62:63], v[130:131]
	v_pk_mul_f32 v[58:59], v[58:59], v[140:141]
	v_pk_mul_f32 v[54:55], v[54:55], v[144:145]
	v_pk_mul_f32 v[64:65], v[64:65], v[132:133]
	v_pk_mul_f32 v[60:61], v[60:61], v[142:143]
	v_pk_mul_f32 v[56:57], v[56:57], v[146:147]
	v_pk_mul_f32 v[52:53], v[52:53], v[174:175]
	v_pk_mul_f32 v[50:51], v[50:51], v[172:173]
	v_pk_mul_f32 v[46:47], v[46:47], v[130:131]
	v_pk_mul_f32 v[42:43], v[42:43], v[140:141]
	v_pk_mul_f32 v[38:39], v[38:39], v[144:145]
	v_pk_mul_f32 v[48:49], v[48:49], v[132:133]
	v_pk_mul_f32 v[44:45], v[44:45], v[142:143]
	v_pk_mul_f32 v[40:41], v[40:41], v[146:147]
	v_pk_mul_f32 v[36:37], v[36:37], v[174:175]
	v_pk_mul_f32 v[34:35], v[34:35], v[172:173]
	v_pk_mul_f32 v[30:31], v[30:31], v[130:131]
	v_pk_mul_f32 v[26:27], v[26:27], v[140:141]
	v_pk_mul_f32 v[22:23], v[22:23], v[144:145]
	v_pk_mul_f32 v[32:33], v[32:33], v[132:133]
	v_pk_mul_f32 v[28:29], v[28:29], v[142:143]
	v_pk_mul_f32 v[24:25], v[24:25], v[146:147]
	v_pk_mul_f32 v[20:21], v[20:21], v[174:175]
	v_pk_mul_f32 v[18:19], v[18:19], v[172:173]
.LBB0_1177:
	v_cndmask_b32_e64 v130, v138, v165, s[6:7]
	s_mul_hi_u32 s12, s79, 0xaaaaaaab
	v_mul_f32_e32 v131, 0xbdd53b94, v130
	s_lshr_b32 s12, s12, 1
	v_fmamk_f32 v66, v66, 0x3dd53b94, v131
	v_fmamk_f32 v68, v68, 0x3dd53b94, v131
	v_fmamk_f32 v70, v70, 0x3dd53b94, v131
	v_fmamk_f32 v72, v72, 0x3dd53b94, v131
	s_mul_i32 s12, s12, 0xfffee000
	v_fmamk_f32 v74, v74, 0x3dd53b94, v131
	v_fmamk_f32 v76, v76, 0x3dd53b94, v131
	v_fmamk_f32 v78, v78, 0x3dd53b94, v131
	v_fmamk_f32 v80, v80, 0x3dd53b94, v131
	v_fmamk_f32 v132, v82, 0x3dd53b94, v131
	v_fmamk_f32 v133, v84, 0x3dd53b94, v131
	v_fmamk_f32 v146, v86, 0x3dd53b94, v131
	v_fmamk_f32 v147, v88, 0x3dd53b94, v131
	v_fmamk_f32 v165, v90, 0x3dd53b94, v131
	v_fmamk_f32 v166, v92, 0x3dd53b94, v131
	v_fmamk_f32 v168, v94, 0x3dd53b94, v131
	v_fmamk_f32 v169, v96, 0x3dd53b94, v131
	v_exp_f32_e32 v171, v66
	v_exp_f32_e32 v224, v68
	v_exp_f32_e32 v225, v70
	v_exp_f32_e32 v226, v72
	v_fmamk_f32 v66, v67, 0x3dd53b94, v131
	v_fmamk_f32 v67, v69, 0x3dd53b94, v131
	v_fmamk_f32 v68, v71, 0x3dd53b94, v131
	v_fmamk_f32 v69, v73, 0x3dd53b94, v131
	v_fmamk_f32 v70, v75, 0x3dd53b94, v131
	v_fmamk_f32 v71, v77, 0x3dd53b94, v131
	v_fmamk_f32 v72, v79, 0x3dd53b94, v131
	v_fmamk_f32 v73, v81, 0x3dd53b94, v131
	v_fmamk_f32 v231, v83, 0x3dd53b94, v131
	v_fmamk_f32 v233, v85, 0x3dd53b94, v131
	v_fmamk_f32 v234, v87, 0x3dd53b94, v131
	v_fmamk_f32 v235, v89, 0x3dd53b94, v131
	v_fmamk_f32 v236, v91, 0x3dd53b94, v131
	v_fmamk_f32 v245, v93, 0x3dd53b94, v131
	v_fmamk_f32 v246, v95, 0x3dd53b94, v131
	v_fmac_f32_e32 v131, 0x3dd53b94, v97
	s_add_i32 s12, s12, 0
	v_exp_f32_e32 v227, v74
	v_exp_f32_e32 v228, v76
	v_exp_f32_e32 v229, v78
	v_exp_f32_e32 v230, v80
	v_exp_f32_e32 v237, v66
	v_exp_f32_e32 v238, v67
	v_exp_f32_e32 v239, v68
	v_exp_f32_e32 v240, v69
	v_exp_f32_e32 v241, v70
	v_exp_f32_e32 v242, v71
	v_exp_f32_e32 v243, v72
	v_exp_f32_e32 v244, v73
	v_add_u32_e32 v196, s16, v159
	v_add_u32_e32 v204, s16, v161
	v_add_u32_e32 v212, s16, v162
	v_add_u32_e32 v220, s16, v163
	ds_read_b128 v[66:69], v196 offset:32768
	ds_read_b128 v[82:85], v204 offset:32768
	ds_read_b128 v[86:89], v212 offset:32768
	ds_read_b128 v[90:93], v220 offset:32768
	ds_read_b128 v[94:97], v196 offset:32896
	ds_read_b128 v[138:141], v204 offset:32896
	ds_read_b128 v[142:145], v212 offset:32896
	ds_read_b128 v[172:175], v220 offset:32896
	ds_read_b128 v[176:179], v158
	ds_read_b128 v[180:183], v196 offset:33024
	ds_read_b128 v[184:187], v158 offset:1024
	ds_read_b128 v[188:191], v204 offset:33024
	ds_read_b128 v[192:195], v158 offset:2048
	ds_read_b128 v[200:203], v212 offset:33024
	ds_read_b128 v[208:211], v158 offset:3072
	s_waitcnt lgkmcnt(14)
	v_mfma_f32_32x32x16_bf16 v[66:81], v[66:69], v[126:129], 0
	ds_read_b128 v[216:219], v220 offset:33024
	s_waitcnt lgkmcnt(13)
	v_mfma_f32_32x32x16_bf16 v[66:81], v[82:85], v[122:125], v[66:81]
	v_mfma_f32_32x32x16_bf16 v[66:81], v[86:89], v[118:121], v[66:81]
	s_waitcnt lgkmcnt(11)
	v_mfma_f32_32x32x16_bf16 v[66:81], v[90:93], v[114:117], v[66:81]
	v_mfma_f32_32x32x16_bf16 v[66:81], v[94:97], v[110:113], v[66:81]
	s_waitcnt lgkmcnt(8)
	v_mfma_f32_32x32x16_bf16 v[66:81], v[138:141], v[106:109], v[66:81]
	ds_read_b128 v[138:141], v196 offset:45056
	v_mfma_f32_32x32x16_bf16 v[66:81], v[142:145], v[102:105], v[66:81]
	ds_read_b128 v[142:145], v204 offset:45056
	v_mfma_f32_32x32x16_bf16 v[66:81], v[172:175], v[98:101], v[66:81]
	ds_read_b128 v[172:175], v212 offset:45056
	s_waitcnt lgkmcnt(3)
	v_mfma_f32_32x32x16_bf16 v[66:81], v[180:183], v[176:179], v[66:81]
	ds_read_b128 v[180:183], v220 offset:45056
	v_mfma_f32_32x32x16_bf16 v[66:81], v[188:191], v[184:187], v[66:81]
	ds_read_b128 v[188:191], v196 offset:45184
	v_mfma_f32_32x32x16_bf16 v[66:81], v[200:203], v[192:195], v[66:81]
	ds_read_b128 v[200:203], v204 offset:45184
	v_mfma_f32_32x32x16_bf16 v[66:81], v[216:219], v[208:211], v[66:81]
	ds_read_b128 v[216:219], v212 offset:45184
	s_waitcnt lgkmcnt(3)
	v_mfma_f32_32x32x16_bf16 v[82:97], v[138:141], v[126:129], 0
	ds_read_b128 v[138:141], v220 offset:45184
	s_add_i32 s78, s78, 2
	s_min_u32 s6, s78, s14
	s_lshl_b32 s7, s6, 6
	s_cmp_lt_u32 s6, 4
	s_cselect_b32 s6, s74, s15
	s_add_i32 s6, s6, s7
	s_mul_hi_i32 s7, s6, 0x1080
	v_mfma_f32_32x32x16_bf16 v[82:97], v[142:145], v[122:125], v[82:97]
	ds_read_b128 v[196:199], v196 offset:45312
	s_mulk_i32 s6, 0x1080
	v_mfma_f32_32x32x16_bf16 v[82:97], v[172:175], v[118:121], v[82:97]
	ds_read_b128 v[204:207], v204 offset:45312
	v_mfma_f32_32x32x16_bf16 v[82:97], v[180:183], v[114:117], v[82:97]
	ds_read_b128 v[212:215], v212 offset:45312
	s_waitcnt lgkmcnt(3)
	v_mfma_f32_32x32x16_bf16 v[82:97], v[188:191], v[110:113], v[82:97]
	ds_read_b128 v[220:223], v220 offset:45312
	s_add_u32 s6, s3, s6
	s_addc_u32 s7, s35, s7
	s_add_i32 s12, s12, s30
	v_mfma_f32_32x32x16_bf16 v[82:97], v[200:203], v[106:109], v[82:97]
	s_add_i32 s12, s12, s8
	s_add_i32 m0, s12, 0x20000
	s_nop 0
	global_load_lds_dwordx4 v232, s[6:7]
	v_mfma_f32_32x32x16_bf16 v[82:97], v[216:219], v[102:105], v[82:97]
	s_add_i32 m0, s12, 0x20400
	v_mfma_f32_32x32x16_bf16 v[82:97], v[138:141], v[98:101], v[82:97]
	global_load_lds_dwordx4 v251, s[6:7]
	s_add_i32 m0, s12, 0x20800
	s_waitcnt lgkmcnt(0)
	v_mfma_f32_32x32x16_bf16 v[82:97], v[196:199], v[176:179], v[82:97]
	v_mfma_f32_32x32x16_bf16 v[82:97], v[204:207], v[184:187], v[82:97]
	global_load_lds_dwordx4 v252, s[6:7]
	v_mfma_f32_32x32x16_bf16 v[82:97], v[212:215], v[192:195], v[82:97]
	v_mfma_f32_32x32x16_bf16 v[82:97], v[220:223], v[208:211], v[82:97]
	v_add_f32_e32 v138, 0, v171
	v_add_f32_e32 v138, v237, v138
	v_add_f32_e32 v138, v224, v138
	v_add_f32_e32 v138, v238, v138
	v_add_f32_e32 v138, v225, v138
	v_add_f32_e32 v138, v239, v138
	v_add_f32_e32 v138, v226, v138
	v_add_f32_e32 v138, v240, v138
	v_add_f32_e32 v138, v227, v138
	v_add_f32_e32 v138, v241, v138
	v_add_f32_e32 v138, v228, v138
	v_add_f32_e32 v138, v242, v138
	v_exp_f32_e32 v132, v132
	v_add_f32_e32 v138, v229, v138
	v_exp_f32_e32 v172, v231
	v_add_f32_e32 v138, v243, v138
	v_exp_f32_e32 v133, v133
	v_add_f32_e32 v138, v230, v138
	v_exp_f32_e32 v173, v233
	v_add_f32_e32 v138, v244, v138
	v_exp_f32_e32 v146, v146
	v_add_f32_e32 v138, v132, v138
	v_exp_f32_e32 v174, v234
	v_add_f32_e32 v138, v172, v138
	v_exp_f32_e32 v147, v147
	v_add_f32_e32 v138, v133, v138
	v_exp_f32_e32 v175, v235
	v_add_f32_e32 v138, v173, v138
	v_exp_f32_e32 v165, v165
	v_add_f32_e32 v138, v146, v138
	v_exp_f32_e32 v176, v236
	v_add_f32_e32 v138, v174, v138
	v_exp_f32_e32 v166, v166
	v_add_f32_e32 v138, v147, v138
	v_exp_f32_e32 v177, v245
	v_add_f32_e32 v138, v175, v138
	v_exp_f32_e32 v168, v168
	v_add_f32_e32 v138, v165, v138
	v_exp_f32_e32 v178, v246
	v_add_f32_e32 v138, v176, v138
	v_exp_f32_e32 v169, v169
	v_add_f32_e32 v138, v166, v138
	v_exp_f32_e32 v131, v131
	v_add_f32_e32 v138, v177, v138
	v_add_f32_e32 v138, v168, v138
	v_add_f32_e32 v138, v178, v138
	v_add_f32_e32 v138, v169, v138
	v_add_f32_e32 v185, v131, v138
	v_mov_b32_e32 v186, v185
	s_nop 1
	v_permlane32_swap_b32_e32 v185, v186
	v_cvt_pk_bf16_f32 v138, v171, v237
	v_cvt_pk_bf16_f32 v139, v224, v238
	v_cvt_pk_bf16_f32 v140, v225, v239
	v_cvt_pk_bf16_f32 v141, v226, v240
	v_cvt_pk_bf16_f32 v142, v227, v241
	v_cvt_pk_bf16_f32 v143, v228, v242
	v_cvt_pk_bf16_f32 v144, v229, v243
	v_cvt_pk_bf16_f32 v145, v230, v244
	v_cvt_pk_bf16_f32 v172, v132, v172
	v_cvt_pk_bf16_f32 v173, v133, v173
	v_cvt_pk_bf16_f32 v174, v146, v174
	v_cvt_pk_bf16_f32 v175, v147, v175
	v_cvt_pk_bf16_f32 v176, v165, v176
	v_cvt_pk_bf16_f32 v177, v166, v177
	v_cvt_pk_bf16_f32 v178, v168, v178
	v_cvt_pk_bf16_f32 v179, v169, v131
	s_nop 0
	v_permlane32_swap_b32_e32 v138, v140
	v_permlane32_swap_b32_e32 v139, v141
	v_permlane32_swap_b32_e32 v142, v144
	v_permlane32_swap_b32_e32 v143, v145
	v_permlane32_swap_b32_e32 v172, v174
	v_permlane32_swap_b32_e32 v173, v175
	v_permlane32_swap_b32_e32 v176, v178
	v_permlane32_swap_b32_e32 v177, v179
	ds_read_b64_tr_b16 v[180:181], v156 offset:0
	ds_read_b64_tr_b16 v[182:183], v156 offset:0x800
	ds_read_b64_tr_b16 v[188:189], v156 offset:0x1000
	ds_read_b64_tr_b16 v[190:191], v156 offset:0x1800
	ds_read_b64_tr_b16 v[192:193], v156 offset:0x2000
	ds_read_b64_tr_b16 v[194:195], v156 offset:0x2800
	ds_read_b64_tr_b16 v[196:197], v156 offset:0x3000
	ds_read_b64_tr_b16 v[198:199], v156 offset:0x3800
	s_nop 0
	s_waitcnt lgkmcnt(4)
	v_mfma_f32_32x32x16_bf16 v[2:17], v[138:141], v[180:183], v[2:17]
	ds_read_b64_tr_b16 v[180:181], v156 offset:0x200
	ds_read_b64_tr_b16 v[182:183], v156 offset:0xa00
	v_mfma_f32_32x32x16_bf16 v[2:17], v[142:145], v[188:191], v[2:17]
	ds_read_b64_tr_b16 v[188:189], v156 offset:0x1200
	ds_read_b64_tr_b16 v[190:191], v156 offset:0x1a00
	s_waitcnt lgkmcnt(4)
	v_mfma_f32_32x32x16_bf16 v[2:17], v[172:175], v[192:195], v[2:17]
	ds_read_b64_tr_b16 v[192:193], v156 offset:0x2200
	ds_read_b64_tr_b16 v[194:195], v156 offset:0x2a00
	ds_read_b64_tr_b16 v[200:201], v156 offset:0x3200
	ds_read_b64_tr_b16 v[202:203], v156 offset:0x3a00
	v_mfma_f32_32x32x16_bf16 v[2:17], v[176:179], v[196:199], v[2:17]
	s_waitcnt lgkmcnt(4)
	v_mfma_f32_32x32x16_bf16 v[50:65], v[138:141], v[180:183], v[50:65]
	ds_read_b64_tr_b16 v[180:181], v156 offset:0x400
	ds_read_b64_tr_b16 v[182:183], v156 offset:0xc00
	v_mfma_f32_32x32x16_bf16 v[50:65], v[142:145], v[188:191], v[50:65]
	ds_read_b64_tr_b16 v[188:189], v156 offset:0x1400
	ds_read_b64_tr_b16 v[190:191], v156 offset:0x1c00
	s_waitcnt lgkmcnt(4)
	v_mfma_f32_32x32x16_bf16 v[50:65], v[172:175], v[192:195], v[50:65]
	ds_read_b64_tr_b16 v[192:193], v156 offset:0x2400
	ds_read_b64_tr_b16 v[194:195], v156 offset:0x2c00
	ds_read_b64_tr_b16 v[196:197], v156 offset:0x3400
	ds_read_b64_tr_b16 v[198:199], v156 offset:0x3c00
	v_mfma_f32_32x32x16_bf16 v[50:65], v[176:179], v[200:203], v[50:65]
	s_waitcnt lgkmcnt(4)
	v_mfma_f32_32x32x16_bf16 v[34:49], v[138:141], v[180:183], v[34:49]
	ds_read_b64_tr_b16 v[180:181], v156 offset:0x600
	ds_read_b64_tr_b16 v[182:183], v156 offset:0xe00
	v_mfma_f32_32x32x16_bf16 v[34:49], v[142:145], v[188:191], v[34:49]
	ds_read_b64_tr_b16 v[188:189], v156 offset:0x1600
	ds_read_b64_tr_b16 v[190:191], v156 offset:0x1e00
	s_waitcnt lgkmcnt(4)
	v_mfma_f32_32x32x16_bf16 v[34:49], v[172:175], v[192:195], v[34:49]
	ds_read_b64_tr_b16 v[192:193], v156 offset:0x2600
	ds_read_b64_tr_b16 v[194:195], v156 offset:0x2e00
	ds_read_b64_tr_b16 v[200:201], v156 offset:0x3600
	ds_read_b64_tr_b16 v[202:203], v156 offset:0x3e00
	v_mfma_f32_32x32x16_bf16 v[34:49], v[176:179], v[196:199], v[34:49]
	s_waitcnt vmcnt(3) lgkmcnt(0)
	s_barrier
	v_mfma_f32_32x32x16_bf16 v[18:33], v[138:141], v[180:183], v[18:33]
	s_mov_b32 m0, s76
	s_nop 0
	global_load_lds_dwordx4 v253, s[10:11]
	s_mov_b32 m0, s77
	v_max_f32_e32 v132, v66, v66
	global_load_lds_dwordx4 v254, s[10:11]
	v_max_f32_e32 v131, v67, v67
	v_max_f32_e32 v131, v132, v131
	v_max3_f32 v131, v131, v68, v69
	v_max3_f32 v131, v131, v70, v71
	v_max3_f32 v131, v131, v72, v73
	v_max3_f32 v131, v131, v74, v75
	v_mfma_f32_32x32x16_bf16 v[18:33], v[142:145], v[188:191], v[18:33]
	v_max3_f32 v131, v131, v76, v77
	v_max3_f32 v131, v131, v78, v79
	v_max3_f32 v131, v131, v80, v81
	v_max3_f32 v131, v131, v82, v83
	v_max3_f32 v131, v131, v84, v85
	v_max3_f32 v131, v131, v86, v87
	v_max3_f32 v131, v131, v88, v89
	v_max3_f32 v131, v131, v90, v91
	v_mfma_f32_32x32x16_bf16 v[18:33], v[172:175], v[192:195], v[18:33]
	v_max3_f32 v131, v131, v92, v93
	v_max3_f32 v131, v131, v94, v95
	v_max3_f32 v131, v131, v96, v97
	v_mov_b32_e32 v132, v131
	s_nop 1
	v_permlane32_swap_b32_e32 v131, v132
	v_max_f32_e32 v132, v132, v132
	v_max_f32_e32 v131, v131, v131
	v_max_f32_e32 v131, v131, v132
	v_max_f32_e32 v133, v130, v130
	v_sub_f32_e32 v132, v131, v130
	v_max_f32_e32 v131, v133, v131
	v_mfma_f32_32x32x16_bf16 v[18:33], v[176:179], v[200:203], v[18:33]
	v_sub_f32_e32 v133, v130, v131
	v_mul_f32_e32 v133, 0x3dd53b94, v133
	v_exp_f32_e32 v133, v133
	v_cmp_ge_f32_e32 vcc, s65, v132
	s_cmp_eq_u64 vcc, exec
	s_cselect_b64 s[6:7], -1, 0
	v_cndmask_b32_e64 v166, v133, 1.0, s[6:7]
	v_cmp_gt_f32_e32 vcc, 1.0, v166
	s_cbranch_vccz .LBB0_1181
	s_and_saveexec_b64 s[10:11], s[4:5]
	ds_write_b32 v155, v166 offset:128
	s_or_b64 exec, exec, s[10:11]
	s_waitcnt lgkmcnt(0)
	v_add_u32_e32 v132, s69, v134
	ds_read_b128 v[138:141], v132 offset:224
	ds_read_b128 v[142:145], v132 offset:192
	ds_read_b128 v[172:175], v132 offset:160
	ds_read_b128 v[176:179], v132 offset:128
	s_waitcnt lgkmcnt(0)
	v_pk_mul_f32 v[14:15], v[14:15], v[138:139]
	v_pk_mul_f32 v[10:11], v[10:11], v[142:143]
	v_pk_mul_f32 v[6:7], v[6:7], v[172:173]
	v_pk_mul_f32 v[16:17], v[16:17], v[140:141]
	v_pk_mul_f32 v[12:13], v[12:13], v[144:145]
	v_pk_mul_f32 v[8:9], v[8:9], v[174:175]
	v_pk_mul_f32 v[4:5], v[4:5], v[178:179]
	v_pk_mul_f32 v[2:3], v[2:3], v[176:177]
	v_pk_mul_f32 v[62:63], v[62:63], v[138:139]
	v_pk_mul_f32 v[58:59], v[58:59], v[142:143]
	v_pk_mul_f32 v[54:55], v[54:55], v[172:173]
	v_pk_mul_f32 v[64:65], v[64:65], v[140:141]
	v_pk_mul_f32 v[60:61], v[60:61], v[144:145]
	v_pk_mul_f32 v[56:57], v[56:57], v[174:175]
	v_pk_mul_f32 v[52:53], v[52:53], v[178:179]
	v_pk_mul_f32 v[50:51], v[50:51], v[176:177]
	v_pk_mul_f32 v[46:47], v[46:47], v[138:139]
	v_pk_mul_f32 v[42:43], v[42:43], v[142:143]
	v_pk_mul_f32 v[38:39], v[38:39], v[172:173]
	v_pk_mul_f32 v[48:49], v[48:49], v[140:141]
	v_pk_mul_f32 v[44:45], v[44:45], v[144:145]
	v_pk_mul_f32 v[40:41], v[40:41], v[174:175]
	v_pk_mul_f32 v[36:37], v[36:37], v[178:179]
	v_pk_mul_f32 v[34:35], v[34:35], v[176:177]
	v_pk_mul_f32 v[30:31], v[30:31], v[138:139]
	v_pk_mul_f32 v[26:27], v[26:27], v[142:143]
	v_pk_mul_f32 v[22:23], v[22:23], v[172:173]
	v_pk_mul_f32 v[32:33], v[32:33], v[140:141]
	v_pk_mul_f32 v[28:29], v[28:29], v[144:145]
	v_pk_mul_f32 v[24:25], v[24:25], v[174:175]
	v_pk_mul_f32 v[20:21], v[20:21], v[178:179]
	v_pk_mul_f32 v[18:19], v[18:19], v[176:177]

.LBB0_1183:
	s_mul_i32 s7, s7, 0x12000
	s_sub_i32 s6, s8, s7
	s_addk_i32 s6, 0x6000
	v_add_u32_e32 v159, s6, v159
	ds_read_b128 v[66:69], v159 offset:32768
	ds_read_b128 v[186:189], v159 offset:32896
	ds_read_b128 v[82:85], v159 offset:45056
	ds_read_b128 v[190:193], v159 offset:33024
	v_add_u32_e32 v161, s6, v161
	s_waitcnt lgkmcnt(0)
	v_mfma_f32_32x32x16_bf16 v[66:81], v[66:69], v[126:129], 0
	v_add_u32_e32 v162, s6, v162
	v_add_u32_e32 v163, s6, v163
	v_exp_f32_e32 v146, v146
	v_exp_f32_e32 v147, v147
	v_exp_f32_e32 v144, v144
	v_exp_f32_e32 v145, v145
	v_exp_f32_e32 v142, v142
	v_mfma_f32_32x32x16_bf16 v[82:97], v[82:85], v[126:129], 0
	ds_read_b128 v[126:129], v161 offset:32768
	ds_read_b128 v[194:197], v161 offset:32896
	ds_read_b128 v[198:201], v161 offset:33024
	v_exp_f32_e32 v136, v136
	v_exp_f32_e32 v137, v137
	v_exp_f32_e32 v132, v132
	v_exp_f32_e32 v133, v133
	v_exp_f32_e32 v130, v130
	s_waitcnt lgkmcnt(0)
	v_mfma_f32_32x32x16_bf16 v[66:81], v[126:129], v[122:125], v[66:81]
	ds_read_b128 v[126:129], v161 offset:45056
	v_exp_f32_e32 v131, v131
	s_waitcnt lgkmcnt(0)
	v_mfma_f32_32x32x16_bf16 v[82:97], v[126:129], v[122:125], v[82:97]
	ds_read_b128 v[122:125], v162 offset:32768
	ds_read_b128 v[126:129], v162 offset:32896
	ds_read_b128 v[202:205], v162 offset:33024
	s_waitcnt lgkmcnt(0)
	v_mfma_f32_32x32x16_bf16 v[66:81], v[122:125], v[118:121], v[66:81]
	ds_read_b128 v[122:125], v162 offset:45056
	s_waitcnt lgkmcnt(0)
	v_mfma_f32_32x32x16_bf16 v[82:97], v[122:125], v[118:121], v[82:97]
	ds_read_b128 v[118:121], v163 offset:32768
	ds_read_b128 v[122:125], v163 offset:32896
	s_waitcnt lgkmcnt(0)
	v_mfma_f32_32x32x16_bf16 v[66:81], v[118:121], v[114:117], v[66:81]
	ds_read_b128 v[118:121], v163 offset:45056
	ds_read_b128 v[206:209], v163 offset:33024
	s_waitcnt lgkmcnt(0)
	v_mfma_f32_32x32x16_bf16 v[82:97], v[118:121], v[114:117], v[82:97]
	ds_read_b128 v[114:117], v159 offset:45184
	ds_read_b128 v[118:121], v159 offset:45312
	v_mfma_f32_32x32x16_bf16 v[66:81], v[186:189], v[110:113], v[66:81]
	s_waitcnt lgkmcnt(0)
	v_mfma_f32_32x32x16_bf16 v[82:97], v[114:117], v[110:113], v[82:97]
	ds_read_b128 v[110:113], v161 offset:45184
	v_mfma_f32_32x32x16_bf16 v[66:81], v[194:197], v[106:109], v[66:81]
	ds_read_b128 v[114:117], v161 offset:45312
	ds_read_b128 v[186:189], v158
	ds_read_b128 v[194:197], v158 offset:1024
	ds_read_b128 v[210:213], v162 offset:45184
	ds_read_b128 v[214:217], v162 offset:45312
	ds_read_b128 v[218:221], v163 offset:45184
	ds_read_b128 v[222:225], v163 offset:45312
	s_waitcnt lgkmcnt(0)
	v_mfma_f32_32x32x16_bf16 v[82:97], v[110:113], v[106:109], v[82:97]
	ds_read_b128 v[106:109], v158 offset:2048
	ds_read_b128 v[110:113], v158 offset:3072
	v_mfma_f32_32x32x16_bf16 v[66:81], v[126:129], v[102:105], v[66:81]
	v_exp_f32_e32 v126, v143
	v_exp_f32_e32 v127, v140
	v_exp_f32_e32 v128, v141
	v_exp_f32_e32 v129, v138
	v_exp_f32_e32 v138, v139
	v_mfma_f32_32x32x16_bf16 v[82:97], v[210:213], v[102:105], v[82:97]
	v_add_f32_e32 v102, 0, v178
	v_add_f32_e32 v102, v182, v102
	v_add_f32_e32 v102, v179, v102
	v_add_f32_e32 v102, v183, v102
	v_add_f32_e32 v102, v180, v102
	v_add_f32_e32 v102, v184, v102
	v_add_f32_e32 v102, v177, v102
	v_mfma_f32_32x32x16_bf16 v[66:81], v[122:125], v[98:101], v[66:81]
	v_add_f32_e32 v102, v181, v102
	v_add_f32_e32 v102, v171, v102
	v_add_f32_e32 v102, v175, v102
	v_mfma_f32_32x32x16_bf16 v[82:97], v[218:221], v[98:101], v[82:97]
	v_add_f32_e32 v98, v172, v102
	v_add_f32_e32 v98, v176, v98
	v_add_f32_e32 v98, v168, v98
	v_add_f32_e32 v98, v173, v98
	v_add_f32_e32 v98, v169, v98
	v_add_f32_e32 v98, v174, v98
	v_add_f32_e32 v98, v146, v98
	v_mfma_f32_32x32x16_bf16 v[66:81], v[190:193], v[186:189], v[66:81]
	v_add_f32_e32 v98, v147, v98
	v_add_f32_e32 v98, v144, v98
	v_add_f32_e32 v98, v145, v98
	v_add_f32_e32 v98, v142, v98
	v_add_f32_e32 v98, v126, v98
	v_add_f32_e32 v98, v127, v98
	v_add_f32_e32 v98, v128, v98
	v_mfma_f32_32x32x16_bf16 v[82:97], v[118:121], v[186:189], v[82:97]
	v_add_f32_e32 v98, v129, v98
	v_add_f32_e32 v98, v138, v98
	v_add_f32_e32 v98, v136, v98
	v_add_f32_e32 v98, v137, v98
	v_add_f32_e32 v98, v132, v98
	v_add_f32_e32 v98, v133, v98
	v_add_f32_e32 v98, v130, v98
	v_mfma_f32_32x32x16_bf16 v[66:81], v[198:201], v[194:197], v[66:81]
	v_add_f32_e32 v98, v131, v98
	v_mov_b32_e32 v99, v98
	v_cvt_pk_bf16_f32 v100, v178, v182
	v_cvt_pk_bf16_f32 v101, v179, v183
	v_cvt_pk_bf16_f32 v102, v180, v184
	v_cvt_pk_bf16_f32 v103, v177, v181
	s_nop 1
	v_permlane32_swap_b32_e32 v98, v99
	v_mfma_f32_32x32x16_bf16 v[82:97], v[114:117], v[194:197], v[82:97]
	v_permlane32_swap_b32_e32 v100, v102
	v_permlane32_swap_b32_e32 v101, v103
	v_cvt_pk_bf16_f32 v114, v171, v175
	v_cvt_pk_bf16_f32 v115, v172, v176
	v_cvt_pk_bf16_f32 v116, v168, v173
	s_waitcnt lgkmcnt(0)
	v_mfma_f32_32x32x16_bf16 v[66:81], v[202:205], v[106:109], v[66:81]
	v_cvt_pk_bf16_f32 v117, v169, v174
	v_cvt_pk_bf16_f32 v104, v146, v147
	v_cvt_pk_bf16_f32 v105, v144, v145
	v_permlane32_swap_b32_e32 v114, v116
	v_permlane32_swap_b32_e32 v115, v117
	v_mfma_f32_32x32x16_bf16 v[82:97], v[214:217], v[106:109], v[82:97]
	v_cvt_pk_bf16_f32 v106, v142, v126
	v_cvt_pk_bf16_f32 v107, v127, v128
	v_cvt_pk_bf16_f32 v118, v129, v138
	v_cvt_pk_bf16_f32 v119, v136, v137
	v_cvt_pk_bf16_f32 v120, v132, v133
	v_cvt_pk_bf16_f32 v121, v130, v131
	s_nop 0
	v_permlane32_swap_b32_e32 v104, v106
	v_mfma_f32_32x32x16_bf16 v[66:81], v[206:209], v[110:113], v[66:81]
	v_permlane32_swap_b32_e32 v105, v107
	v_permlane32_swap_b32_e32 v118, v120
	v_permlane32_swap_b32_e32 v119, v121
	v_mfma_f32_32x32x16_bf16 v[82:97], v[222:225], v[110:113], v[82:97]
	ds_read_b64_tr_b16 v[108:109], v160 offset:0
	ds_read_b64_tr_b16 v[110:111], v160 offset:0x800
	ds_read_b64_tr_b16 v[122:123], v160 offset:0x1000
	ds_read_b64_tr_b16 v[124:125], v160 offset:0x1800
	ds_read_b64_tr_b16 v[126:127], v160 offset:0x2000
	ds_read_b64_tr_b16 v[128:129], v160 offset:0x2800
	ds_read_b64_tr_b16 v[130:131], v160 offset:0x3000
	ds_read_b64_tr_b16 v[132:133], v160 offset:0x3800
	s_nop 0
	s_waitcnt lgkmcnt(4)
	v_mfma_f32_32x32x16_bf16 v[2:17], v[100:103], v[108:111], v[2:17]
	ds_read_b64_tr_b16 v[108:109], v160 offset:0x200
	ds_read_b64_tr_b16 v[110:111], v160 offset:0xa00
	v_mfma_f32_32x32x16_bf16 v[2:17], v[114:117], v[122:125], v[2:17]
	ds_read_b64_tr_b16 v[122:123], v160 offset:0x1200
	ds_read_b64_tr_b16 v[124:125], v160 offset:0x1a00
	s_waitcnt lgkmcnt(4)
	v_mfma_f32_32x32x16_bf16 v[2:17], v[104:107], v[126:129], v[2:17]
	ds_read_b64_tr_b16 v[126:127], v160 offset:0x2200
	ds_read_b64_tr_b16 v[128:129], v160 offset:0x2a00
	ds_read_b64_tr_b16 v[136:137], v160 offset:0x3200
	ds_read_b64_tr_b16 v[138:139], v160 offset:0x3a00
	v_mfma_f32_32x32x16_bf16 v[2:17], v[118:121], v[130:133], v[2:17]
	s_waitcnt lgkmcnt(4)
	v_mfma_f32_32x32x16_bf16 v[50:65], v[100:103], v[108:111], v[50:65]
	ds_read_b64_tr_b16 v[108:109], v160 offset:0x400
	ds_read_b64_tr_b16 v[110:111], v160 offset:0xc00
	v_mfma_f32_32x32x16_bf16 v[50:65], v[114:117], v[122:125], v[50:65]
	ds_read_b64_tr_b16 v[122:123], v160 offset:0x1400
	ds_read_b64_tr_b16 v[124:125], v160 offset:0x1c00
	s_waitcnt lgkmcnt(4)
	v_mfma_f32_32x32x16_bf16 v[50:65], v[104:107], v[126:129], v[50:65]
	ds_read_b64_tr_b16 v[126:127], v160 offset:0x2400
	ds_read_b64_tr_b16 v[128:129], v160 offset:0x2c00
	ds_read_b64_tr_b16 v[130:131], v160 offset:0x3400
	ds_read_b64_tr_b16 v[132:133], v160 offset:0x3c00
	v_mfma_f32_32x32x16_bf16 v[50:65], v[118:121], v[136:139], v[50:65]
	s_waitcnt lgkmcnt(4)
	v_mfma_f32_32x32x16_bf16 v[34:49], v[100:103], v[108:111], v[34:49]
	ds_read_b64_tr_b16 v[108:109], v160 offset:0x600
	ds_read_b64_tr_b16 v[110:111], v160 offset:0xe00
	v_mfma_f32_32x32x16_bf16 v[34:49], v[114:117], v[122:125], v[34:49]
	ds_read_b64_tr_b16 v[122:123], v160 offset:0x1600
	ds_read_b64_tr_b16 v[124:125], v160 offset:0x1e00
	s_waitcnt lgkmcnt(4)
	v_mfma_f32_32x32x16_bf16 v[34:49], v[104:107], v[126:129], v[34:49]
	ds_read_b64_tr_b16 v[126:127], v160 offset:0x2600
	ds_read_b64_tr_b16 v[128:129], v160 offset:0x2e00
	ds_read_b64_tr_b16 v[136:137], v160 offset:0x3600
	ds_read_b64_tr_b16 v[138:139], v160 offset:0x3e00
	v_mfma_f32_32x32x16_bf16 v[34:49], v[118:121], v[130:133], v[34:49]
	s_waitcnt lgkmcnt(4)
	v_mfma_f32_32x32x16_bf16 v[18:33], v[100:103], v[108:111], v[18:33]
	v_max_f32_e32 v112, v67, v67
	v_max_f32_e32 v113, v66, v66
	v_max_f32_e32 v112, v113, v112
	v_max3_f32 v112, v112, v68, v69
	v_max3_f32 v112, v112, v70, v71
	v_max3_f32 v100, v112, v72, v73
	v_max3_f32 v100, v100, v74, v75
	v_max3_f32 v100, v100, v76, v77
	v_mfma_f32_32x32x16_bf16 v[18:33], v[114:117], v[122:125], v[18:33]
	v_max3_f32 v100, v100, v78, v79
	v_max3_f32 v100, v100, v80, v81
	v_max3_f32 v100, v100, v82, v83
	v_max3_f32 v100, v100, v84, v85
	v_max3_f32 v100, v100, v86, v87
	v_max3_f32 v100, v100, v88, v89
	v_max3_f32 v100, v100, v90, v91
	v_max3_f32 v100, v100, v92, v93
	s_waitcnt lgkmcnt(0)
	v_mfma_f32_32x32x16_bf16 v[18:33], v[104:107], v[126:129], v[18:33]
	v_max3_f32 v100, v100, v94, v95
	v_max3_f32 v100, v100, v96, v97
	v_mov_b32_e32 v101, v100
	s_nop 1
	v_permlane32_swap_b32_e32 v100, v101
	v_max_f32_e32 v101, v101, v101
	v_max_f32_e32 v100, v100, v100
	v_max_f32_e32 v100, v100, v101
	v_max_f32_e32 v101, v165, v165
	v_max_f32_e32 v101, v101, v100
	v_sub_f32_e32 v102, v100, v165
	v_mfma_f32_32x32x16_bf16 v[18:33], v[118:121], v[136:139], v[18:33]
	v_sub_f32_e32 v100, v165, v101
	v_mul_f32_e32 v100, 0x3dd53b94, v100
	v_exp_f32_e32 v100, v100
	v_cmp_ge_f32_e32 vcc, s65, v102
	s_cmp_eq_u64 vcc, exec
	s_cselect_b64 s[6:7], -1, 0
	s_waitcnt vmcnt(0) lgkmcnt(0)
	s_barrier
	v_cndmask_b32_e64 v100, v100, 1.0, s[6:7]
	v_cmp_gt_f32_e32 vcc, 1.0, v100
	s_cbranch_vccz .LBB0_1187
	s_and_saveexec_b64 s[8:9], s[4:5]
	ds_write_b32 v155, v100 offset:128
	s_or_b64 exec, exec, s[8:9]
	s_waitcnt lgkmcnt(0)
	v_add_u32_e32 v114, s69, v134
	ds_read_b128 v[102:105], v114 offset:224
	ds_read_b128 v[106:109], v114 offset:192
	ds_read_b128 v[110:113], v114 offset:160
	ds_read_b128 v[114:117], v114 offset:128
	s_waitcnt lgkmcnt(0)
	v_pk_mul_f32 v[14:15], v[14:15], v[102:103]
	v_pk_mul_f32 v[10:11], v[10:11], v[106:107]
	v_pk_mul_f32 v[6:7], v[6:7], v[110:111]
	v_pk_mul_f32 v[16:17], v[16:17], v[104:105]
	v_pk_mul_f32 v[12:13], v[12:13], v[108:109]
	v_pk_mul_f32 v[8:9], v[8:9], v[112:113]
	v_pk_mul_f32 v[4:5], v[4:5], v[116:117]
	v_pk_mul_f32 v[2:3], v[2:3], v[114:115]
	v_pk_mul_f32 v[62:63], v[62:63], v[102:103]
	v_pk_mul_f32 v[58:59], v[58:59], v[106:107]
	v_pk_mul_f32 v[54:55], v[54:55], v[110:111]
	v_pk_mul_f32 v[64:65], v[64:65], v[104:105]
	v_pk_mul_f32 v[60:61], v[60:61], v[108:109]
	v_pk_mul_f32 v[56:57], v[56:57], v[112:113]
	v_pk_mul_f32 v[52:53], v[52:53], v[116:117]
	v_pk_mul_f32 v[50:51], v[50:51], v[114:115]
	v_pk_mul_f32 v[46:47], v[46:47], v[102:103]
	v_pk_mul_f32 v[42:43], v[42:43], v[106:107]
	v_pk_mul_f32 v[38:39], v[38:39], v[110:111]
	v_pk_mul_f32 v[48:49], v[48:49], v[104:105]
	v_pk_mul_f32 v[44:45], v[44:45], v[108:109]
	v_pk_mul_f32 v[40:41], v[40:41], v[112:113]
	v_pk_mul_f32 v[36:37], v[36:37], v[116:117]
	v_pk_mul_f32 v[34:35], v[34:35], v[114:115]
	v_pk_mul_f32 v[30:31], v[30:31], v[102:103]
	v_pk_mul_f32 v[26:27], v[26:27], v[106:107]
	v_pk_mul_f32 v[22:23], v[22:23], v[110:111]
	v_pk_mul_f32 v[32:33], v[32:33], v[104:105]
	v_pk_mul_f32 v[28:29], v[28:29], v[108:109]
	v_pk_mul_f32 v[24:25], v[24:25], v[112:113]
	v_pk_mul_f32 v[20:21], v[20:21], v[116:117]
	v_pk_mul_f32 v[18:19], v[18:19], v[114:115]
.LBB0_1187:
	v_cndmask_b32_e64 v101, v101, v165, s[6:7]
	v_mul_f32_e32 v101, 0xbdd53b94, v101
	v_fmamk_f32 v66, v66, 0x3dd53b94, v101
	v_fmamk_f32 v67, v67, 0x3dd53b94, v101
	v_fmamk_f32 v68, v68, 0x3dd53b94, v101
	v_fmamk_f32 v69, v69, 0x3dd53b94, v101
	v_fmamk_f32 v70, v70, 0x3dd53b94, v101
	v_fmamk_f32 v71, v71, 0x3dd53b94, v101
	v_fmamk_f32 v72, v72, 0x3dd53b94, v101
	v_fmamk_f32 v73, v73, 0x3dd53b94, v101
	v_fmamk_f32 v74, v74, 0x3dd53b94, v101
	v_fmamk_f32 v75, v75, 0x3dd53b94, v101
	v_fmamk_f32 v76, v76, 0x3dd53b94, v101
	v_fmamk_f32 v77, v77, 0x3dd53b94, v101
	v_fmamk_f32 v78, v78, 0x3dd53b94, v101
	v_fmamk_f32 v79, v79, 0x3dd53b94, v101
	v_fmamk_f32 v80, v80, 0x3dd53b94, v101
	v_fmamk_f32 v81, v81, 0x3dd53b94, v101
	v_fmamk_f32 v82, v82, 0x3dd53b94, v101
	v_fmamk_f32 v83, v83, 0x3dd53b94, v101
	v_fmamk_f32 v84, v84, 0x3dd53b94, v101
	v_fmamk_f32 v85, v85, 0x3dd53b94, v101
	v_fmamk_f32 v86, v86, 0x3dd53b94, v101
	v_fmamk_f32 v87, v87, 0x3dd53b94, v101
	v_fmamk_f32 v88, v88, 0x3dd53b94, v101
	v_fmamk_f32 v89, v89, 0x3dd53b94, v101
	v_fmamk_f32 v90, v90, 0x3dd53b94, v101
	v_fmamk_f32 v91, v91, 0x3dd53b94, v101
	v_fmamk_f32 v92, v92, 0x3dd53b94, v101
	v_fmamk_f32 v93, v93, 0x3dd53b94, v101
	v_fmamk_f32 v94, v94, 0x3dd53b94, v101
	v_fmamk_f32 v95, v95, 0x3dd53b94, v101
	v_fmamk_f32 v96, v96, 0x3dd53b94, v101
	v_fmac_f32_e32 v101, 0x3dd53b94, v97
	v_exp_f32_e32 v97, v66
	v_exp_f32_e32 v102, v67
	v_exp_f32_e32 v103, v68
	v_exp_f32_e32 v69, v69
	v_exp_f32_e32 v70, v70
	v_add_f32_e32 v66, 0, v97
	v_exp_f32_e32 v71, v71
	v_add_f32_e32 v66, v102, v66
	v_exp_f32_e32 v72, v72
	v_add_f32_e32 v66, v103, v66
	v_exp_f32_e32 v73, v73
	v_add_f32_e32 v66, v69, v66
	v_exp_f32_e32 v74, v74
	v_add_f32_e32 v66, v70, v66
	v_exp_f32_e32 v75, v75
	v_add_f32_e32 v66, v71, v66
	v_exp_f32_e32 v76, v76
	v_add_f32_e32 v66, v72, v66
	v_exp_f32_e32 v77, v77
	v_add_f32_e32 v66, v73, v66
	v_exp_f32_e32 v78, v78
	v_add_f32_e32 v66, v74, v66
	v_exp_f32_e32 v79, v79
	v_add_f32_e32 v66, v75, v66
	v_exp_f32_e32 v80, v80
	v_add_f32_e32 v66, v76, v66
	v_exp_f32_e32 v81, v81
	v_add_f32_e32 v66, v77, v66
	v_exp_f32_e32 v82, v82
	v_add_f32_e32 v66, v78, v66
	v_exp_f32_e32 v83, v83
	v_add_f32_e32 v66, v79, v66
	v_exp_f32_e32 v84, v84
	v_add_f32_e32 v66, v80, v66
	v_exp_f32_e32 v85, v85
	v_add_f32_e32 v66, v81, v66
	v_exp_f32_e32 v86, v86
	v_add_f32_e32 v66, v82, v66
	v_exp_f32_e32 v87, v87
	v_add_f32_e32 v66, v83, v66
	v_exp_f32_e32 v88, v88
	v_add_f32_e32 v66, v84, v66
	v_exp_f32_e32 v89, v89
	v_add_f32_e32 v66, v85, v66
	v_exp_f32_e32 v90, v90
	v_add_f32_e32 v66, v86, v66
	v_exp_f32_e32 v91, v91
	v_add_f32_e32 v66, v87, v66
	v_exp_f32_e32 v92, v92
	v_add_f32_e32 v66, v88, v66
	v_exp_f32_e32 v93, v93
	v_add_f32_e32 v66, v89, v66
	v_exp_f32_e32 v94, v94
	v_add_f32_e32 v66, v90, v66
	v_exp_f32_e32 v95, v95
	v_add_f32_e32 v66, v91, v66
	v_exp_f32_e32 v96, v96
	v_add_f32_e32 v66, v92, v66
	v_exp_f32_e32 v101, v101
	v_add_f32_e32 v66, v93, v66
	v_add_f32_e32 v66, v94, v66
	v_add_f32_e32 v66, v95, v66
	v_add_f32_e32 v66, v96, v66
	v_add_f32_e32 v66, v101, v66
	v_mov_b32_e32 v67, v66
	s_nop 1
	v_permlane32_swap_b32_e32 v66, v67
	v_cvt_pk_bf16_f32 v68, v97, v102
	v_cvt_pk_bf16_f32 v69, v103, v69
	v_cvt_pk_bf16_f32 v70, v70, v71
	v_cvt_pk_bf16_f32 v71, v72, v73
	v_cvt_pk_bf16_f32 v72, v74, v75
	v_cvt_pk_bf16_f32 v73, v76, v77
	v_cvt_pk_bf16_f32 v74, v78, v79
	v_cvt_pk_bf16_f32 v75, v80, v81
	v_cvt_pk_bf16_f32 v76, v82, v83
	v_cvt_pk_bf16_f32 v77, v84, v85
	v_cvt_pk_bf16_f32 v78, v86, v87
	v_cvt_pk_bf16_f32 v79, v88, v89
	v_cvt_pk_bf16_f32 v80, v90, v91
	v_cvt_pk_bf16_f32 v81, v92, v93
	v_cvt_pk_bf16_f32 v82, v94, v95
	v_cvt_pk_bf16_f32 v83, v96, v101
	s_nop 0
	v_permlane32_swap_b32_e32 v68, v70
	v_permlane32_swap_b32_e32 v69, v71
	v_permlane32_swap_b32_e32 v72, v74
	v_permlane32_swap_b32_e32 v73, v75
	v_permlane32_swap_b32_e32 v76, v78
	v_permlane32_swap_b32_e32 v77, v79
	v_permlane32_swap_b32_e32 v80, v82
	v_permlane32_swap_b32_e32 v81, v83
	ds_read_b64_tr_b16 v[84:85], v156 offset:0
	ds_read_b64_tr_b16 v[86:87], v156 offset:0x800
	ds_read_b64_tr_b16 v[88:89], v156 offset:0x1000
	ds_read_b64_tr_b16 v[90:91], v156 offset:0x1800
	ds_read_b64_tr_b16 v[92:93], v156 offset:0x2000
	ds_read_b64_tr_b16 v[94:95], v156 offset:0x2800
	ds_read_b64_tr_b16 v[102:103], v156 offset:0x3000
	ds_read_b64_tr_b16 v[104:105], v156 offset:0x3800
	s_nop 0
	s_waitcnt lgkmcnt(4)
	v_mfma_f32_32x32x16_bf16 v[2:17], v[68:71], v[84:87], v[2:17]
	ds_read_b64_tr_b16 v[84:85], v156 offset:0x200
	ds_read_b64_tr_b16 v[86:87], v156 offset:0xa00
	v_mfma_f32_32x32x16_bf16 v[2:17], v[72:75], v[88:91], v[2:17]
	ds_read_b64_tr_b16 v[88:89], v156 offset:0x1200
	ds_read_b64_tr_b16 v[90:91], v156 offset:0x1a00
	s_waitcnt lgkmcnt(4)
	v_mfma_f32_32x32x16_bf16 v[2:17], v[76:79], v[92:95], v[2:17]
	ds_read_b64_tr_b16 v[92:93], v156 offset:0x2200
	ds_read_b64_tr_b16 v[94:95], v156 offset:0x2a00
	ds_read_b64_tr_b16 v[106:107], v156 offset:0x3200
	ds_read_b64_tr_b16 v[108:109], v156 offset:0x3a00
	v_mfma_f32_32x32x16_bf16 v[2:17], v[80:83], v[102:105], v[2:17]
	s_waitcnt lgkmcnt(4)
	v_mfma_f32_32x32x16_bf16 v[50:65], v[68:71], v[84:87], v[50:65]
	ds_read_b64_tr_b16 v[84:85], v156 offset:0x400
	ds_read_b64_tr_b16 v[86:87], v156 offset:0xc00
	v_mfma_f32_32x32x16_bf16 v[50:65], v[72:75], v[88:91], v[50:65]
	ds_read_b64_tr_b16 v[88:89], v156 offset:0x1400
	ds_read_b64_tr_b16 v[90:91], v156 offset:0x1c00
	s_waitcnt lgkmcnt(4)
	v_mfma_f32_32x32x16_bf16 v[50:65], v[76:79], v[92:95], v[50:65]
	ds_read_b64_tr_b16 v[92:93], v156 offset:0x2400
	ds_read_b64_tr_b16 v[94:95], v156 offset:0x2c00
	ds_read_b64_tr_b16 v[102:103], v156 offset:0x3400
	ds_read_b64_tr_b16 v[104:105], v156 offset:0x3c00
	v_mfma_f32_32x32x16_bf16 v[50:65], v[80:83], v[106:109], v[50:65]
	s_waitcnt lgkmcnt(4)
	v_mfma_f32_32x32x16_bf16 v[34:49], v[68:71], v[84:87], v[34:49]
	ds_read_b64_tr_b16 v[84:85], v156 offset:0x600
	ds_read_b64_tr_b16 v[86:87], v156 offset:0xe00
	v_mfma_f32_32x32x16_bf16 v[34:49], v[72:75], v[88:91], v[34:49]
	ds_read_b64_tr_b16 v[88:89], v156 offset:0x1600
	ds_read_b64_tr_b16 v[90:91], v156 offset:0x1e00
	s_waitcnt lgkmcnt(4)
	v_mfma_f32_32x32x16_bf16 v[34:49], v[76:79], v[92:95], v[34:49]
	ds_read_b64_tr_b16 v[92:93], v156 offset:0x2600
	ds_read_b64_tr_b16 v[94:95], v156 offset:0x2e00
	ds_read_b64_tr_b16 v[106:107], v156 offset:0x3600
	ds_read_b64_tr_b16 v[108:109], v156 offset:0x3e00
	v_mfma_f32_32x32x16_bf16 v[34:49], v[80:83], v[102:105], v[34:49]
	s_waitcnt lgkmcnt(4)
	v_mfma_f32_32x32x16_bf16 v[18:33], v[68:71], v[84:87], v[18:33]
	v_mfma_f32_32x32x16_bf16 v[18:33], v[72:75], v[88:91], v[18:33]
	s_waitcnt lgkmcnt(0)
	v_mfma_f32_32x32x16_bf16 v[18:33], v[76:79], v[92:95], v[18:33]
	v_mfma_f32_32x32x16_bf16 v[18:33], v[80:83], v[106:109], v[18:33]
	s_and_saveexec_b64 s[6:7], s[4:5]
	s_cbranch_execz .LBB0_1164
	v_add_f32_e32 v68, v98, v99
	v_fmac_f32_e32 v68, v157, v166
	v_add_f32_e32 v66, v66, v67
	v_fmac_f32_e32 v66, v68, v100
	ds_write_b32 v155, v66
	s_branch .LBB0_1164
